# P2 rewrite with write-through sc1 stores
# baseline (speedup 1.0000x reference)
; __device__ __forceinline__ void postproj_row(int R, int lane, const bf16* __restrict__ proj, const float* __restrict__ conv_w, const float* __restrict__ g_conv, ...
;     const bf16* pr = proj + (size_t)R * DINP;
;     const bool meta = R >= M; const int b = meta ? 0 : R / S, t = meta ? 0 : R % S, pos = meta ? R - M : t + NMETA;
;     {
;         const u32x2 w = *(const u32x2*)(pr + O_KV + lane * 4);
;         float f[4] = {__uint_as_float(w.x << 16), __uint_as_float(w.x & 0xffff0000u), __uint_as_float(w.y << 16), __uint_as_float(w.y & 0xffff0000u)};
;         const float ss = wave_sum(f[0] * f[0] + f[1] * f[1] + f[2] * f[2] + f[3] * f[3]);
;         const float rstd = rsqrtf(ss * (1.f / KVL) + EPS);
;         const f32x4 g = *(const f32x4*)(g_kv + lane * 4);
;         u32x2 o; o.x = pk2(f[0] * rstd * g.x, f[1] * rstd * g.y); o.y = pk2(f[2] * rstd * g.z, f[3] * rstd * g.w);
;         *(u32x2*)(kvn + (size_t)R * KVL + lane * 4) = o;
;     }
;     if (lane < 32) {
;         const float x1 = bf2f(pr[O_R + lane]), x2 = bf2f(pr[O_R + 32 + lane]);
;         const float cs = cosT[pos * 32 + lane], sn = sinT[pos * 32 + lane];
;         const bf16 o1 = f2bf(x1 * cs - x2 * sn), o2 = f2bf(x1 * sn + x2 * cs);
;         if (!meta) { bf16* d = kpe + (size_t)(b * LP + pos) * ROPE; d[lane] = o1; d[32 + lane] = o2; }
;         else { bf16* d0 = kpe + (size_t)(0 * LP + pos) * ROPE; bf16* d1 = kpe + (size_t)(1 * LP + pos) * ROPE; d0[lane] = o1; d0[32 + lane] = o2; d1[lane] = o1; d1[32 + lane] = o2; }
;     }
;     if (meta) return;
;     {
;         float f[8]; unpack8(*(const u32x4*)(pr + O_Q + lane * 8), f);
;         float ss = 0.f;
; #pragma unroll
;         for (int i = 0; i < 8; ++i) ss += f[i] * f[i];
;         const float rstd = rsqrtf(wave_sum(ss) * (1.f / QL) + EPS);
;         const f32x4 g0 = *(const f32x4*)(g_q + lane * 8), g1 = *(const f32x4*)(g_q + lane * 8 + 4);
;         u32x4 o; o.x = pk2(f[0] * rstd * g0.x, f[1] * rstd * g0.y); o.y = pk2(f[2] * rstd * g0.z, f[3] * rstd * g0.w);
;         o.z = pk2(f[4] * rstd * g1.x, f[5] * rstd * g1.y); o.w = pk2(f[6] * rstd * g1.z, f[7] * rstd * g1.w);
;         *(u32x4*)(qn + (size_t)R * QL + lane * 8) = o;
;     }
;     {
;         const int r1 = (t >= 1) ? R - 1 : M + 15, r2 = (t >= 2) ? R - 2 : (t == 1 ? M + 15 : M + 14);
;         const bf16* p1 = proj + (size_t)r1 * DINP; const bf16* p2 = proj + (size_t)r2 * DINP;
.Lp2_loop:
	s_lshl_b32 s43, s42, 13
	s_add_u32 s48, s44, s43
	s_addc_u32 s49, s45, 0
	s_add_u32 s50, s48, 0x1000
	s_addc_u32 s51, s49, 0
	s_and_b32 s52, s42, 0xfff
	s_lshr_b32 s53, s42, 12
	s_add_i32 s54, s42, -1
	s_cmp_eq_u32 s52, 0
	s_cselect_b32 s54, 0x200f, s54
	s_add_i32 s56, s42, -2
	s_add_i32 s43, s52, 0x200e
	s_cmp_lt_u32 s52, 2
	s_cselect_b32 s56, s43, s56
	s_lshl_b32 s54, s54, 13
	s_lshl_b32 s56, s56, 13
	s_add_u32 s54, s54, 0x800
	s_add_u32 s56, s56, 0x800
	s_add_u32 s54, s44, s54
	s_addc_u32 s55, s45, 0
	s_add_u32 s56, s44, s56
	s_addc_u32 s57, s45, 0
	s_add_i32 s43, s52, 16
	s_lshl_b32 s58, s43, 7
	s_add_u32 s58, s40, s58
	s_addc_u32 s59, s41, 0
	s_add_u32 s4, s58, 0x100000
	s_addc_u32 s5, s59, 0
	global_load_dwordx4 v[108:111], v2, s[54:55]
	global_load_dwordx4 v[112:115], v2, s[54:55] offset:16
	global_load_dwordx4 v[116:119], v2, s[54:55] offset:2048
	global_load_dwordx4 v[120:123], v2, s[54:55] offset:2064
	global_load_dwordx4 v[124:127], v2, s[56:57]
	global_load_dwordx4 v[128:131], v2, s[56:57] offset:16
	global_load_dwordx4 v[132:135], v2, s[56:57] offset:2048
	global_load_dwordx4 v[136:139], v2, s[56:57] offset:2064
	global_load_dwordx4 v[84:87], v2, s[48:49]
	global_load_dwordx4 v[88:91], v2, s[48:49] offset:16
	global_load_dwordx4 v[92:95], v2, s[48:49] offset:2048
	global_load_dwordx4 v[96:99], v2, s[48:49] offset:2064
	global_load_dwordx4 v[100:103], v2, s[50:51]
	global_load_dwordx4 v[104:107], v2, s[50:51] offset:16
	global_load_dwordx4 v[140:143], v3, s[50:51] offset:2048
	global_load_dwordx2 v[144:145], v4, s[50:51] offset:3072
	global_load_ushort v146, v6, s[50:51] offset:3584
	global_load_ushort v147, v6, s[50:51] offset:3648
	global_load_dword v148, v5, s[58:59]
	global_load_dword v149, v5, s[4:5]
	s_lshl_b32 s43, s42, 12
	s_add_u32 s6, s46, s43
	s_addc_u32 s7, s47, 0
	s_lshl_b32 s43, s42, 10
	s_add_u32 s24, s34, s43
	s_addc_u32 s25, s35, 0
	s_lshl_b32 s43, s42, 9
	s_add_u32 s8, s38, s43
	s_addc_u32 s9, s39, 0
	s_mulk_i32 s53, 0x1080
	s_add_i32 s53, s53, s52
	s_add_i32 s53, s53, 16
	s_lshl_b32 s53, s53, 7
	s_add_u32 s10, s26, s53
	s_addc_u32 s11, s27, 0
	v_mov_b32_e32 v206, 0x358637bd
	s_waitcnt vmcnt(0)
	v_lshlrev_b32_e32 v186, 16, v140
	v_and_b32_e32 v187, 0xffff0000, v140
	v_lshlrev_b32_e32 v188, 16, v141
	v_and_b32_e32 v189, 0xffff0000, v141
	v_lshlrev_b32_e32 v190, 16, v142
	v_and_b32_e32 v191, 0xffff0000, v142
	v_lshlrev_b32_e32 v192, 16, v143
	v_and_b32_e32 v193, 0xffff0000, v143
	v_mul_f32_e32 v194, v186, v186
	v_fmac_f32_e32 v194, v187, v187
	v_fmac_f32_e32 v194, v188, v188
	v_fmac_f32_e32 v194, v189, v189
	v_fmac_f32_e32 v194, v190, v190
	v_fmac_f32_e32 v194, v191, v191
	v_fmac_f32_e32 v194, v192, v192
	v_fmac_f32_e32 v194, v193, v193
	v_lshlrev_b32_e32 v196, 16, v144
	v_and_b32_e32 v197, 0xffff0000, v144
	v_lshlrev_b32_e32 v198, 16, v145
	v_and_b32_e32 v199, 0xffff0000, v145
	v_mul_f32_e32 v195, v196, v196
	v_fmac_f32_e32 v195, v197, v197
	v_fmac_f32_e32 v195, v198, v198
	v_fmac_f32_e32 v195, v199, v199
	s_nop 1
	v_add_f32_dpp v194, v194, v194 quad_perm:[1,0,3,2] row_mask:0xf bank_mask:0xf
	v_add_f32_dpp v195, v195, v195 quad_perm:[1,0,3,2] row_mask:0xf bank_mask:0xf
	s_nop 1
	v_add_f32_dpp v194, v194, v194 quad_perm:[2,3,0,1] row_mask:0xf bank_mask:0xf
	v_add_f32_dpp v195, v195, v195 quad_perm:[2,3,0,1] row_mask:0xf bank_mask:0xf
	s_nop 1
	v_add_f32_dpp v194, v194, v194 row_half_mirror row_mask:0xf bank_mask:0xf
	v_add_f32_dpp v195, v195, v195 row_half_mirror row_mask:0xf bank_mask:0xf
	s_nop 1
	v_add_f32_dpp v194, v194, v194 row_mirror row_mask:0xf bank_mask:0xf
	v_add_f32_dpp v195, v195, v195 row_mirror row_mask:0xf bank_mask:0xf
	s_nop 1
	v_add_f32_dpp v194, v194, v194 row_bcast:15 row_mask:0xa bank_mask:0xf
	v_add_f32_dpp v195, v195, v195 row_bcast:15 row_mask:0xa bank_mask:0xf
	s_nop 1
	v_add_f32_dpp v194, v194, v194 row_bcast:31 row_mask:0xc bank_mask:0xf
	v_add_f32_dpp v195, v195, v195 row_bcast:31 row_mask:0xc bank_mask:0xf
	v_lshlrev_b32_e32 v150, 16, v92
	v_and_b32_e32 v151, 0xffff0000, v92
	v_lshlrev_b32_e32 v152, 16, v100
	v_and_b32_e32 v153, 0xffff0000, v100
	v_pk_mul_f32 v[150:151], v[150:151], v[152:153]
	v_lshlrev_b32_e32 v152, 16, v108
	v_and_b32_e32 v153, 0xffff0000, v108
	v_lshlrev_b32_e32 v154, 16, v116
	v_and_b32_e32 v155, 0xffff0000, v116
	v_pk_mul_f32 v[152:153], v[152:153], v[154:155]
	v_lshlrev_b32_e32 v154, 16, v124
	v_and_b32_e32 v155, 0xffff0000, v124
	v_lshlrev_b32_e32 v156, 16, v132
	v_and_b32_e32 v157, 0xffff0000, v132
	v_pk_mul_f32 v[154:155], v[154:155], v[156:157]
	v_pk_mul_f32 v[152:153], v[52:53], v[152:153]
	v_pk_fma_f32 v[152:153], v[68:69], v[150:151], v[152:153]
	v_pk_fma_f32 v[152:153], v[36:37], v[154:155], v[152:153]
	v_lshlrev_b32_e32 v156, 16, v84
	v_and_b32_e32 v157, 0xffff0000, v84
	v_pk_mul_f32 v[160:161], v[156:157], v[152:153]
	v_mul_f32_e32 v158, v160, v160
	v_fmac_f32_e32 v158, v161, v161
	v_lshlrev_b32_e32 v150, 16, v93
	v_and_b32_e32 v151, 0xffff0000, v93
	v_lshlrev_b32_e32 v152, 16, v101
	v_and_b32_e32 v153, 0xffff0000, v101
	v_pk_mul_f32 v[150:151], v[150:151], v[152:153]
	v_lshlrev_b32_e32 v152, 16, v109
	v_and_b32_e32 v153, 0xffff0000, v109
	v_lshlrev_b32_e32 v154, 16, v117
	v_and_b32_e32 v155, 0xffff0000, v117
	v_pk_mul_f32 v[152:153], v[152:153], v[154:155]
	v_lshlrev_b32_e32 v154, 16, v125
	v_and_b32_e32 v155, 0xffff0000, v125
	v_lshlrev_b32_e32 v156, 16, v133
	v_and_b32_e32 v157, 0xffff0000, v133
	v_pk_mul_f32 v[154:155], v[154:155], v[156:157]
	v_pk_mul_f32 v[152:153], v[54:55], v[152:153]
	v_pk_fma_f32 v[152:153], v[70:71], v[150:151], v[152:153]
	v_pk_fma_f32 v[152:153], v[38:39], v[154:155], v[152:153]
	v_lshlrev_b32_e32 v156, 16, v85
; __device__ __forceinline__ void postproj_row(int R, int lane, const bf16* __restrict__ proj, const float* __restrict__ conv_w, const float* __restrict__ g_conv, ...
;     ...
;             float bg[8], cg0[8], ui0[8], cg1[8], ui1[8], cg2[8], ui2[8];
;             unpack8(*(const u32x4*)(pr + c), bg); unpack8(*(const u32x4*)(pr + O_C + c), cg0); unpack8(*(const u32x4*)(pr + O_U + c), ui0);
;             unpack8(*(const u32x4*)(p1 + O_C + c), cg1); unpack8(*(const u32x4*)(p1 + O_U + c), ui1);
;             unpack8(*(const u32x4*)(p2 + O_C + c), cg2); unpack8(*(const u32x4*)(p2 + O_U + c), ui2);
; #pragma unroll
;             for (int i = 0; i < 8; ++i) {
;                 const float y = conv_w[2 * DCONV + c + i] * (cg0[i] * ui0[i]) + conv_w[1 * DCONV + c + i] * (cg1[i] * ui1[i]) + conv_w[0 * DCONV + c + i] * (cg2[i] * ui2[i]);
;                 const float o = bg[i] * y; v[hh * 8 + i] = o; ss += o * o;
;             }
;         }
	v_and_b32_e32 v157, 0xffff0000, v85
	v_pk_mul_f32 v[162:163], v[156:157], v[152:153]
	v_fmac_f32_e32 v158, v162, v162
	v_fmac_f32_e32 v158, v163, v163
	v_lshlrev_b32_e32 v150, 16, v94
	v_and_b32_e32 v151, 0xffff0000, v94
	v_lshlrev_b32_e32 v152, 16, v102
	v_and_b32_e32 v153, 0xffff0000, v102
	v_pk_mul_f32 v[150:151], v[150:151], v[152:153]
	v_lshlrev_b32_e32 v152, 16, v110
	v_and_b32_e32 v153, 0xffff0000, v110
	v_lshlrev_b32_e32 v154, 16, v118
	v_and_b32_e32 v155, 0xffff0000, v118
	v_pk_mul_f32 v[152:153], v[152:153], v[154:155]
	v_lshlrev_b32_e32 v154, 16, v126
	v_and_b32_e32 v155, 0xffff0000, v126
	v_lshlrev_b32_e32 v156, 16, v134
	v_and_b32_e32 v157, 0xffff0000, v134
	v_pk_mul_f32 v[154:155], v[154:155], v[156:157]
	v_pk_mul_f32 v[152:153], v[56:57], v[152:153]
	v_pk_fma_f32 v[152:153], v[72:73], v[150:151], v[152:153]
	v_pk_fma_f32 v[152:153], v[40:41], v[154:155], v[152:153]
	v_lshlrev_b32_e32 v156, 16, v86
	v_and_b32_e32 v157, 0xffff0000, v86
	v_pk_mul_f32 v[164:165], v[156:157], v[152:153]
	v_fmac_f32_e32 v158, v164, v164
	v_fmac_f32_e32 v158, v165, v165
	v_lshlrev_b32_e32 v150, 16, v95
	v_and_b32_e32 v151, 0xffff0000, v95
	v_lshlrev_b32_e32 v152, 16, v103
	v_and_b32_e32 v153, 0xffff0000, v103
	v_pk_mul_f32 v[150:151], v[150:151], v[152:153]
	v_lshlrev_b32_e32 v152, 16, v111
	v_and_b32_e32 v153, 0xffff0000, v111
	v_lshlrev_b32_e32 v154, 16, v119
	v_and_b32_e32 v155, 0xffff0000, v119
	v_pk_mul_f32 v[152:153], v[152:153], v[154:155]
	v_lshlrev_b32_e32 v154, 16, v127
	v_and_b32_e32 v155, 0xffff0000, v127
	v_lshlrev_b32_e32 v156, 16, v135
	v_and_b32_e32 v157, 0xffff0000, v135
	v_pk_mul_f32 v[154:155], v[154:155], v[156:157]
	v_pk_mul_f32 v[152:153], v[58:59], v[152:153]
	v_pk_fma_f32 v[152:153], v[74:75], v[150:151], v[152:153]
	v_pk_fma_f32 v[152:153], v[42:43], v[154:155], v[152:153]
	v_lshlrev_b32_e32 v156, 16, v87
	v_and_b32_e32 v157, 0xffff0000, v87
	v_pk_mul_f32 v[166:167], v[156:157], v[152:153]
	v_fmac_f32_e32 v158, v166, v166
	v_fmac_f32_e32 v158, v167, v167
	v_lshlrev_b32_e32 v150, 16, v96
	v_and_b32_e32 v151, 0xffff0000, v96
	v_lshlrev_b32_e32 v152, 16, v104
	v_and_b32_e32 v153, 0xffff0000, v104
	v_pk_mul_f32 v[150:151], v[150:151], v[152:153]
	v_lshlrev_b32_e32 v152, 16, v112
	v_and_b32_e32 v153, 0xffff0000, v112
	v_lshlrev_b32_e32 v154, 16, v120
	v_and_b32_e32 v155, 0xffff0000, v120
	v_pk_mul_f32 v[152:153], v[152:153], v[154:155]
	v_lshlrev_b32_e32 v154, 16, v128
	v_and_b32_e32 v155, 0xffff0000, v128
	v_lshlrev_b32_e32 v156, 16, v136
	v_and_b32_e32 v157, 0xffff0000, v136
	v_pk_mul_f32 v[154:155], v[154:155], v[156:157]
	v_pk_mul_f32 v[152:153], v[60:61], v[152:153]
	v_pk_fma_f32 v[152:153], v[76:77], v[150:151], v[152:153]
	v_pk_fma_f32 v[152:153], v[44:45], v[154:155], v[152:153]
	v_lshlrev_b32_e32 v156, 16, v88
	v_and_b32_e32 v157, 0xffff0000, v88
	v_pk_mul_f32 v[168:169], v[156:157], v[152:153]
	v_fmac_f32_e32 v158, v168, v168
	v_fmac_f32_e32 v158, v169, v169
	v_lshlrev_b32_e32 v150, 16, v97
	v_and_b32_e32 v151, 0xffff0000, v97
	v_lshlrev_b32_e32 v152, 16, v105
	v_and_b32_e32 v153, 0xffff0000, v105
	v_pk_mul_f32 v[150:151], v[150:151], v[152:153]
	v_lshlrev_b32_e32 v152, 16, v113
	v_and_b32_e32 v153, 0xffff0000, v113
	v_lshlrev_b32_e32 v154, 16, v121
	v_and_b32_e32 v155, 0xffff0000, v121
	v_pk_mul_f32 v[152:153], v[152:153], v[154:155]
	v_lshlrev_b32_e32 v154, 16, v129
	v_and_b32_e32 v155, 0xffff0000, v129
	v_lshlrev_b32_e32 v156, 16, v137
	v_and_b32_e32 v157, 0xffff0000, v137
	v_pk_mul_f32 v[154:155], v[154:155], v[156:157]
	v_pk_mul_f32 v[152:153], v[62:63], v[152:153]
	v_pk_fma_f32 v[152:153], v[78:79], v[150:151], v[152:153]
	v_pk_fma_f32 v[152:153], v[46:47], v[154:155], v[152:153]
	v_lshlrev_b32_e32 v156, 16, v89
	v_and_b32_e32 v157, 0xffff0000, v89
	v_pk_mul_f32 v[170:171], v[156:157], v[152:153]
	v_fmac_f32_e32 v158, v170, v170
	v_fmac_f32_e32 v158, v171, v171
	v_lshlrev_b32_e32 v150, 16, v98
	v_and_b32_e32 v151, 0xffff0000, v98
	v_lshlrev_b32_e32 v152, 16, v106
	v_and_b32_e32 v153, 0xffff0000, v106
	v_pk_mul_f32 v[150:151], v[150:151], v[152:153]
	v_lshlrev_b32_e32 v152, 16, v114
	v_and_b32_e32 v153, 0xffff0000, v114
	v_lshlrev_b32_e32 v154, 16, v122
	v_and_b32_e32 v155, 0xffff0000, v122
	v_pk_mul_f32 v[152:153], v[152:153], v[154:155]
	v_lshlrev_b32_e32 v154, 16, v130
	v_and_b32_e32 v155, 0xffff0000, v130
	v_lshlrev_b32_e32 v156, 16, v138
	v_and_b32_e32 v157, 0xffff0000, v138
	v_pk_mul_f32 v[154:155], v[154:155], v[156:157]
	v_pk_mul_f32 v[152:153], v[64:65], v[152:153]
	v_pk_fma_f32 v[152:153], v[80:81], v[150:151], v[152:153]
	v_pk_fma_f32 v[152:153], v[48:49], v[154:155], v[152:153]
	v_lshlrev_b32_e32 v156, 16, v90
	v_and_b32_e32 v157, 0xffff0000, v90
	v_pk_mul_f32 v[172:173], v[156:157], v[152:153]
	v_fmac_f32_e32 v158, v172, v172
	v_fmac_f32_e32 v158, v173, v173
	v_lshlrev_b32_e32 v150, 16, v99
	v_and_b32_e32 v151, 0xffff0000, v99
	v_lshlrev_b32_e32 v152, 16, v107
	v_and_b32_e32 v153, 0xffff0000, v107
	v_pk_mul_f32 v[150:151], v[150:151], v[152:153]
	v_lshlrev_b32_e32 v152, 16, v115
	v_and_b32_e32 v153, 0xffff0000, v115
	v_lshlrev_b32_e32 v154, 16, v123
	v_and_b32_e32 v155, 0xffff0000, v123
	v_pk_mul_f32 v[152:153], v[152:153], v[154:155]
	v_lshlrev_b32_e32 v154, 16, v131
	v_and_b32_e32 v155, 0xffff0000, v131
	v_lshlrev_b32_e32 v156, 16, v139
	v_and_b32_e32 v157, 0xffff0000, v139
	v_pk_mul_f32 v[154:155], v[154:155], v[156:157]
	v_pk_mul_f32 v[152:153], v[66:67], v[152:153]
	v_pk_fma_f32 v[152:153], v[82:83], v[150:151], v[152:153]
	v_pk_fma_f32 v[152:153], v[50:51], v[154:155], v[152:153]
	v_lshlrev_b32_e32 v156, 16, v91
	v_and_b32_e32 v157, 0xffff0000, v91
	v_pk_mul_f32 v[174:175], v[156:157], v[152:153]
; __device__ __forceinline__ void postproj_row(int R, int lane, const bf16* __restrict__ proj, const float* __restrict__ conv_w, const float* __restrict__ g_conv, ...
;     ...
;         const float ss = wave_sum(f[0] * f[0] + f[1] * f[1] + f[2] * f[2] + f[3] * f[3]);
;         const float rstd = rsqrtf(ss * (1.f / KVL) + EPS);
;         const f32x4 g = *(const f32x4*)(g_kv + lane * 4);
;         u32x2 o; o.x = pk2(f[0] * rstd * g.x, f[1] * rstd * g.y); o.y = pk2(f[2] * rstd * g.z, f[3] * rstd * g.w);
;         *(u32x2*)(kvn + (size_t)R * KVL + lane * 4) = o;
;     }
;     if (lane < 32) {
;         const float x1 = bf2f(pr[O_R + lane]), x2 = bf2f(pr[O_R + 32 + lane]);
;         const float cs = cosT[pos * 32 + lane], sn = sinT[pos * 32 + lane];
;         const bf16 o1 = f2bf(x1 * cs - x2 * sn), o2 = f2bf(x1 * sn + x2 * cs);
;         if (!meta) { bf16* d = kpe + (size_t)(b * LP + pos) * ROPE; d[lane] = o1; d[32 + lane] = o2; }
;         else { bf16* d0 = kpe + (size_t)(0 * LP + pos) * ROPE; bf16* d1 = kpe + (size_t)(1 * LP + pos) * ROPE; d0[lane] = o1; d0[32 + lane] = o2; d1[lane] = o1; d1[32 + lane] = o2; }
;     }
;     if (meta) return;
;     {
;         float f[8]; unpack8(*(const u32x4*)(pr + O_Q + lane * 8), f);
;         float ss = 0.f;
; #pragma unroll
;         for (int i = 0; i < 8; ++i) ss += f[i] * f[i];
;         const float rstd = rsqrtf(wave_sum(ss) * (1.f / QL) + EPS);
;         const f32x4 g0 = *(const f32x4*)(g_q + lane * 8), g1 = *(const f32x4*)(g_q + lane * 8 + 4);
;         u32x4 o; o.x = pk2(f[0] * rstd * g0.x, f[1] * rstd * g0.y); o.y = pk2(f[2] * rstd * g0.z, f[3] * rstd * g0.w);
;         o.z = pk2(f[4] * rstd * g1.x, f[5] * rstd * g1.y); o.w = pk2(f[6] * rstd * g1.z, f[7] * rstd * g1.w);
;         *(u32x4*)(qn + (size_t)R * QL + lane * 8) = o;
;     }
;     {
;         const int r1 = (t >= 1) ? R - 1 : M + 15, r2 = (t >= 2) ? R - 2 : (t == 1 ? M + 15 : M + 14);
;         const bf16* p1 = proj + (size_t)r1 * DINP; const bf16* p2 = proj + (size_t)r2 * DINP;
;         const int c0 = lane * 16;
;         float v[16]; float ss = 0.f;
; #pragma unroll
;         for (int hh = 0; hh < 2; ++hh) {
;             const int c = c0 + hh * 8;
;             float bg[8], cg0[8], ui0[8], cg1[8], ui1[8], cg2[8], ui2[8];
;             unpack8(*(const u32x4*)(pr + c), bg); unpack8(*(const u32x4*)(pr + O_C + c), cg0); unpack8(*(const u32x4*)(pr + O_U + c), ui0);
	v_fmac_f32_e32 v158, v174, v174
	v_fmac_f32_e32 v158, v175, v175
	v_readlane_b32 s43, v194, 63
	v_readlane_b32 s53, v195, 63
	s_nop 0
	v_add_f32_dpp v158, v158, v158 quad_perm:[1,0,3,2] row_mask:0xf bank_mask:0xf
	v_mov_b32_e32 v151, s43
	v_mov_b32_e32 v152, s53
	v_add_f32_dpp v158, v158, v158 quad_perm:[2,3,0,1] row_mask:0xf bank_mask:0xf
	v_fmamk_f32 v151, v151, 0x3b000000, v206
	v_fmamk_f32 v152, v152, 0x3b800000, v206
	v_fmamk_f32 v158, v158, 0x3c800000, v206
	v_rsq_f32_e32 v151, v151
	v_rsq_f32_e32 v152, v152
	v_rsq_f32_e32 v158, v158
	s_nop 0
	v_mov_b32_e32 v159, v158
	v_mul_f32_e32 v186, v151, v186
	v_mul_f32_e32 v187, v151, v187
	v_mul_f32_e32 v188, v151, v188
	v_mul_f32_e32 v189, v151, v189
	v_mul_f32_e32 v190, v151, v190
	v_mul_f32_e32 v191, v151, v191
	v_mul_f32_e32 v192, v151, v192
	v_mul_f32_e32 v193, v151, v193
	v_mul_f32_e32 v186, v12, v186
	v_mul_f32_e32 v187, v13, v187
	v_mul_f32_e32 v188, v14, v188
	v_mul_f32_e32 v189, v15, v189
	v_mul_f32_e32 v190, v16, v190
	v_mul_f32_e32 v191, v17, v191
	v_mul_f32_e32 v192, v18, v192
	v_mul_f32_e32 v193, v19, v193
	v_cvt_pk_bf16_f32 v200, v186, v187
	v_cvt_pk_bf16_f32 v201, v188, v189
	v_cvt_pk_bf16_f32 v202, v190, v191
	v_cvt_pk_bf16_f32 v203, v192, v193
	global_store_dwordx4 v3, v[200:203], s[24:25] sc1
	v_mul_f32_e32 v196, v152, v196
	v_mul_f32_e32 v197, v152, v197
	v_mul_f32_e32 v198, v152, v198
	v_mul_f32_e32 v199, v152, v199
	v_mul_f32_e32 v196, v8, v196
	v_mul_f32_e32 v197, v9, v197
	v_mul_f32_e32 v198, v10, v198
	v_mul_f32_e32 v199, v11, v199
	v_cvt_pk_bf16_f32 v204, v196, v197
	v_cvt_pk_bf16_f32 v205, v198, v199
	global_store_dwordx2 v4, v[204:205], s[8:9] sc1
	v_pk_mul_f32 v[160:161], v[160:161], v[158:159]
	v_pk_mul_f32 v[162:163], v[162:163], v[158:159]
	v_pk_mul_f32 v[164:165], v[164:165], v[158:159]
	v_pk_mul_f32 v[166:167], v[166:167], v[158:159]
	v_pk_mul_f32 v[168:169], v[168:169], v[158:159]
	v_pk_mul_f32 v[170:171], v[170:171], v[158:159]
	v_pk_mul_f32 v[172:173], v[172:173], v[158:159]
	v_pk_mul_f32 v[174:175], v[174:175], v[158:159]
	v_pk_mul_f32 v[160:161], v[160:161], v[20:21]
	v_pk_mul_f32 v[162:163], v[162:163], v[22:23]
	v_pk_mul_f32 v[164:165], v[164:165], v[24:25]
	v_pk_mul_f32 v[166:167], v[166:167], v[26:27]
	v_pk_mul_f32 v[168:169], v[168:169], v[28:29]
	v_pk_mul_f32 v[170:171], v[170:171], v[30:31]
	v_pk_mul_f32 v[172:173], v[172:173], v[32:33]
	v_pk_mul_f32 v[174:175], v[174:175], v[34:35]
	v_cvt_pk_bf16_f32 v178, v160, v161
	v_cvt_pk_bf16_f32 v179, v162, v163
	v_cvt_pk_bf16_f32 v180, v164, v165
	v_cvt_pk_bf16_f32 v181, v166, v167
	v_cvt_pk_bf16_f32 v182, v168, v169
	v_cvt_pk_bf16_f32 v183, v170, v171
	v_cvt_pk_bf16_f32 v184, v172, v173
	v_cvt_pk_bf16_f32 v185, v174, v175
	global_store_dwordx4 v2, v[178:181], s[6:7] sc1
	global_store_dwordx4 v2, v[182:185], s[6:7] offset:16 sc1
	v_lshlrev_b32_e32 v146, 16, v146
	v_lshlrev_b32_e32 v147, 16, v147
	v_mul_f32_e32 v153, v149, v147
	v_mul_f32_e32 v154, v148, v147
	v_fma_f32 v153, v148, v146, -v153
	v_fmac_f32_e32 v154, v149, v146
	v_cvt_pk_bf16_f32 v155, v153, v154
	s_mov_b32 exec_hi, 0
	global_store_short v6, v155, s[10:11] sc1
	global_store_short_d16_hi v6, v155, s[10:11] offset:64 sc1
	s_mov_b32 exec_hi, -1
	s_add_i32 s42, s42, s30
	s_cmpk_lt_i32 s42, 0x2000
	s_cbranch_scc1 .Lp2_loop
.Lp2_meta_chk:
	s_cmpk_lt_i32 s42, 0x2010
	s_cbranch_scc0 .LBB0_400
	s_lshl_b32 s43, s42, 13
	s_add_u32 s50, s44, s43
	s_addc_u32 s51, s45, 0
	s_add_u32 s50, s50, 0x1000
	s_addc_u32 s51, s51, 0
	s_sub_i32 s52, s42, 0x2000
	s_lshl_b32 s53, s52, 7
	s_add_u32 s58, s40, s53
	s_addc_u32 s59, s41, 0
	s_add_u32 s4, s58, 0x100000
	s_addc_u32 s5, s59, 0
	global_load_dwordx2 v[144:145], v4, s[50:51] offset:3072
	global_load_ushort v146, v6, s[50:51] offset:3584
	global_load_ushort v147, v6, s[50:51] offset:3648
	global_load_dword v148, v5, s[58:59]
	global_load_dword v149, v5, s[4:5]
	s_lshl_b32 s43, s42, 9
	s_add_u32 s8, s38, s43
	s_addc_u32 s9, s39, 0
	s_add_u32 s10, s26, s53
	s_addc_u32 s11, s27, 0
	s_add_u32 s6, s10, 0x84000
	s_addc_u32 s7, s11, 0
	v_mov_b32_e32 v206, 0x358637bd
	s_waitcnt vmcnt(0)
	v_lshlrev_b32_e32 v196, 16, v144
	v_and_b32_e32 v197, 0xffff0000, v144
	v_lshlrev_b32_e32 v198, 16, v145
	v_and_b32_e32 v199, 0xffff0000, v145
	v_mul_f32_e32 v195, v196, v196
	v_fmac_f32_e32 v195, v197, v197
	v_fmac_f32_e32 v195, v198, v198
	v_fmac_f32_e32 v195, v199, v199
	s_nop 1
	v_add_f32_dpp v195, v195, v195 quad_perm:[1,0,3,2] row_mask:0xf bank_mask:0xf
	s_nop 1
	v_add_f32_dpp v195, v195, v195 quad_perm:[2,3,0,1] row_mask:0xf bank_mask:0xf
	s_nop 1
	v_add_f32_dpp v195, v195, v195 row_half_mirror row_mask:0xf bank_mask:0xf
	s_nop 1
	v_add_f32_dpp v195, v195, v195 row_mirror row_mask:0xf bank_mask:0xf
	s_nop 1
	v_add_f32_dpp v195, v195, v195 row_bcast:15 row_mask:0xa bank_mask:0xf
	s_nop 1
	v_add_f32_dpp v195, v195, v195 row_bcast:31 row_mask:0xc bank_mask:0xf
	s_nop 1
	v_readlane_b32 s53, v195, 63
	s_nop 1
	v_mov_b32_e32 v152, s53
	v_fmamk_f32 v152, v152, 0x3b800000, v206
	v_rsq_f32_e32 v152, v152
	s_nop 0
	v_mul_f32_e32 v196, v152, v196
	v_mul_f32_e32 v197, v152, v197
	v_mul_f32_e32 v198, v152, v198
	v_mul_f32_e32 v199, v152, v199
	v_mul_f32_e32 v196, v8, v196
	v_mul_f32_e32 v197, v9, v197
	v_mul_f32_e32 v198, v10, v198
	v_mul_f32_e32 v199, v11, v199
	v_cvt_pk_bf16_f32 v204, v196, v197
	v_cvt_pk_bf16_f32 v205, v198, v199
	global_store_dwordx2 v4, v[204:205], s[8:9] sc1
	v_lshlrev_b32_e32 v146, 16, v146
	v_lshlrev_b32_e32 v147, 16, v147
	v_mul_f32_e32 v153, v149, v147
	v_mul_f32_e32 v154, v148, v147
	v_fma_f32 v153, v148, v146, -v153
	v_fmac_f32_e32 v154, v149, v146
	v_cvt_pk_bf16_f32 v155, v153, v154
	s_mov_b32 exec_hi, 0
	global_store_short v6, v155, s[10:11] sc1
	global_store_short_d16_hi v6, v155, s[10:11] offset:64 sc1
	global_store_short v6, v155, s[6:7] sc1
	global_store_short_d16_hi v6, v155, s[6:7] offset:64 sc1
	s_mov_b32 exec_hi, -1
	s_add_i32 s42, s42, s30
	s_branch .Lp2_meta_chk
